# scan chunk loop: direct role dispatch for the sequential and elementwise waves
# baseline (speedup 1.0000x reference)
.LBB0_952:
	s_cmp_eq_u32 s24, 0
	s_cbranch_scc1 .Lscan_fast_seq
	s_cmp_eq_u32 s24, 7
	s_cbranch_scc1 .Lscan_fast_seq
	s_cmp_eq_u32 s24, 3
	s_cbranch_scc1 .Lscan_fast_e2
	s_cmp_eq_u32 s24, 6
	s_cbranch_scc1 .Lscan_fast_e2
	s_cmp_eq_u32 s24, 2
	s_cbranch_scc1 .LBB0_974
	s_cmp_eq_u32 s24, 5
	s_cbranch_scc1 .LBB0_974
	s_mov_b64 s[12:13], -1
	s_mov_b64 s[6:7], 0
	s_cmp_lt_i32 s24, 3
	s_mov_b64 s[4:5], 0
	s_mov_b64 s[10:11], 0
	s_mov_b64 s[8:9], 0
	s_cbranch_scc1 .LBB0_969
	s_mov_b64 vcc, -1
	s_cmp_gt_i32 s24, 5
	s_mov_b64 s[12:13], 0
	s_cbranch_scc0 .LBB0_956
	s_mov_b64 s[12:13], -1
	s_mov_b64 vcc, 0
	s_cmp_gt_i32 s24, 6
	s_cbranch_scc0 .LBB0_956
	s_cmp_lg_u32 s24, 7
	s_mov_b64 s[12:13], 0
	s_mov_b64 s[4:5], -1
	s_cselect_b64 s[10:11], -1, 0

.Lscan_fast_e2:
	s_and_b32 s10, s84, 1
	v_cndmask_b32_e64 v0, 0, 1, s[90:91]
	v_cmp_eq_u32_e32 vcc, s10, v0
	s_mov_b64 s[10:11], -1
	s_cbranch_vccz .LBB0_964
	s_cmpk_gt_u32 s84, 0xff
	s_cbranch_scc1 .LBB0_963
	v_add_u32_e32 v58, s29, v129
	s_mul_i32 s10, s84, 0xab
	s_waitcnt lgkmcnt(3)
	v_and_b32_e32 v60, 0xffff0000, v176
	v_lshlrev_b32_e32 v61, 16, v176
	v_lshlrev_b32_e32 v62, 16, v177
	v_and_b32_e32 v63, 0xffff0000, v177
	s_waitcnt lgkmcnt(2)
	v_lshlrev_b32_e32 v64, 16, v192
	v_and_b32_e32 v66, 0xffff0000, v192
	v_lshlrev_b32_e32 v68, 16, v193
	v_and_b32_e32 v70, 0xffff0000, v193
	s_waitcnt lgkmcnt(0)
	v_lshlrev_b32_e32 v72, 16, v200
	v_and_b32_e32 v73, 0xffff0000, v200
	v_lshlrev_b32_e32 v74, 16, v201
	v_and_b32_e32 v75, 0xffff0000, v201
	s_bfe_u32 s10, s10, 0x70009
	s_mul_i32 s10, s10, 3
	v_mul_f32_e32 v60, v60, v61
	s_sub_i32 s10, s84, s10
	v_lshlrev_b32_e32 v65, 16, v184
	v_and_b32_e32 v67, 0xffff0000, v184
	s_waitcnt lgkmcnt(3)
	v_lshlrev_b32_e32 v76, 16, v178
	v_and_b32_e32 v77, 0xffff0000, v178
	v_lshlrev_b32_e32 v78, 16, v179
	v_and_b32_e32 v12, 0xffff0000, v179
	s_waitcnt lgkmcnt(0)
	v_lshlrev_b32_e32 v83, 16, v202
	v_and_b32_e32 v84, 0xffff0000, v202
	v_lshlrev_b32_e32 v51, 16, v203
	v_and_b32_e32 v11, 0xffff0000, v203
	v_rcp_f32_e32 v97, v61
	v_rcp_f32_e32 v61, v60
	s_and_b32 s10, s10, 0xff
	v_mul_f32_e32 v65, v65, v64
	v_add_f32_e32 v64, -1.0, v64
	v_mul_f32_e32 v67, v67, v66
	v_add_f32_e32 v66, -1.0, v66
	s_mulk_i32 s10, 0x5300
	s_waitcnt vmcnt(0)
	v_fma_f32 v64, v152, v64, 1.0
	v_fma_f32 v66, v152, v66, 1.0
	s_add_i32 s10, s10, 0
	v_mul_f32_e32 v64, v64, v72
	v_mul_f32_e32 v66, v66, v73
	v_mul_f32_e32 v60, v60, v62
	v_lshlrev_b32_e32 v69, 16, v185
	v_mul_f32_e32 v65, v97, v65
	v_mul_f32_e32 v64, v97, v64
	v_cvt_pk_bf16_f32 v72, v65, v64
	v_add_u32_e32 v97, s10, v127
	v_mul_f32_e32 v67, v61, v67
	v_mul_f32_e32 v61, v61, v66
	v_cvt_pk_bf16_f32 v66, v67, v61
	v_rcp_f32_e32 v62, v60
	v_and_b32_e32 v71, 0xffff0000, v185
	v_lshlrev_b32_e32 v79, 16, v194
	v_lshlrev_b32_e32 v80, 16, v186
	v_and_b32_e32 v81, 0xffff0000, v194
	v_and_b32_e32 v82, 0xffff0000, v186
	v_lshlrev_b32_e32 v15, 16, v195
	v_lshlrev_b32_e32 v49, 16, v187
	v_and_b32_e32 v7, 0xffff0000, v195
	v_and_b32_e32 v10, 0xffff0000, v187
	s_waitcnt lgkmcnt(3)
	v_lshlrev_b32_e32 v85, 16, v180
	v_and_b32_e32 v50, 0xffff0000, v180
	v_lshlrev_b32_e32 v9, 16, v181
	v_and_b32_e32 v4, 0xffff0000, v181
	s_waitcnt lgkmcnt(2)
	v_lshlrev_b32_e32 v86, 16, v196
	s_waitcnt lgkmcnt(1)
	v_lshlrev_b32_e32 v87, 16, v188
	v_and_b32_e32 v13, 0xffff0000, v196
	v_and_b32_e32 v14, 0xffff0000, v188
	v_lshlrev_b32_e32 v5, 16, v197
	v_lshlrev_b32_e32 v6, 16, v189
	v_and_b32_e32 v0, 0xffff0000, v197
	v_and_b32_e32 v2, 0xffff0000, v189
	s_waitcnt lgkmcnt(0)
	v_lshlrev_b32_e32 v88, 16, v204
	v_and_b32_e32 v48, 0xffff0000, v204
	v_lshlrev_b32_e32 v8, 16, v205
	v_and_b32_e32 v3, 0xffff0000, v205
	ds_write_b16 v97, v72 offset:5632
	ds_write_b16_d16_hi v97, v72 offset:7936
	ds_write_b16 v97, v66 offset:5776
	ds_write_b16_d16_hi v97, v66 offset:8080
	v_mul_f32_e32 v66, v69, v68
	v_add_f32_e32 v68, -1.0, v68
	v_mul_f32_e32 v60, v60, v63
	v_fma_f32 v68, v152, v68, 1.0
	v_rcp_f32_e32 v63, v60
	v_mul_f32_e32 v68, v68, v74
	v_add_f32_e32 v69, -1.0, v70
	v_mul_f32_e32 v66, v62, v66
	v_mul_f32_e32 v62, v62, v68
	v_cvt_pk_bf16_f32 v68, v66, v62
	v_fma_f32 v69, v152, v69, 1.0
	ds_write_b16 v97, v68 offset:5920
	ds_write_b16_d16_hi v97, v68 offset:8224
	v_mul_f32_e32 v68, v71, v70
	v_mul_f32_e32 v69, v69, v75
	v_mul_f32_e32 v68, v68, v63
	v_mul_f32_e32 v63, v63, v69
	v_cvt_pk_bf16_f32 v69, v68, v63
	v_mul_f32_e32 v60, v60, v76
	ds_write_b16 v97, v69 offset:6064
	ds_write_b16_d16_hi v97, v69 offset:8368
	v_rcp_f32_e32 v69, v60
	v_add_f32_e32 v71, -1.0, v79
	v_fma_f32 v71, v152, v71, 1.0
	v_mul_f32_e32 v70, v80, v79
	v_mul_f32_e32 v71, v71, v83
	v_mul_f32_e32 v70, v69, v70
	v_mul_f32_e32 v69, v69, v71
	v_cvt_pk_bf16_f32 v71, v70, v69
	v_mul_f32_e32 v60, v60, v77
	ds_write_b16 v97, v71 offset:6208
	ds_write_b16_d16_hi v97, v71 offset:8512
	v_rcp_f32_e32 v71, v60
	v_add_f32_e32 v73, -1.0, v81
	v_fma_f32 v73, v152, v73, 1.0
	v_mul_f32_e32 v72, v82, v81
	v_mul_f32_e32 v73, v73, v84
	v_mul_f32_e32 v72, v71, v72
	v_mul_f32_e32 v71, v71, v73
	v_cvt_pk_bf16_f32 v73, v72, v71
	v_mul_f32_e32 v60, v60, v78
	ds_write_b16 v97, v73 offset:6352
	ds_write_b16_d16_hi v97, v73 offset:8656
	v_rcp_f32_e32 v73, v60
	v_mul_f32_e32 v49, v49, v15
	v_add_f32_e32 v15, -1.0, v15
	v_fma_f32 v15, v152, v15, 1.0
	v_mul_f32_e32 v15, v15, v51
	v_mul_f32_e32 v49, v49, v73
	v_mul_f32_e32 v15, v73, v15
	v_cvt_pk_bf16_f32 v51, v49, v15
	v_mul_f32_e32 v12, v60, v12
	ds_write_b16 v97, v51 offset:6496
	ds_write_b16_d16_hi v97, v51 offset:8800
	v_rcp_f32_e32 v51, v12
	v_mul_f32_e32 v10, v10, v7
	v_add_f32_e32 v7, -1.0, v7
	v_fma_f32 v7, v152, v7, 1.0
	v_mul_f32_e32 v7, v7, v11
	v_mul_f32_e32 v10, v10, v51
	v_mul_f32_e32 v7, v51, v7
	v_cvt_pk_bf16_f32 v11, v10, v7
	ds_write_b16 v97, v11 offset:6640
	ds_write_b16_d16_hi v97, v11 offset:8944
	v_mul_f32_e32 v11, v12, v85
	v_rcp_f32_e32 v12, v11
	v_mul_f32_e32 v11, v11, v50
	v_mul_f32_e32 v9, v11, v9
	v_rcp_f32_e32 v50, v11
	v_rcp_f32_e32 v11, v9
	v_add_f32_e32 v60, -1.0, v86
	v_mul_f32_e32 v14, v14, v13
	v_add_f32_e32 v13, -1.0, v13
	v_mul_f32_e32 v6, v6, v5
	v_add_f32_e32 v5, -1.0, v5
	v_fma_f32 v60, v152, v60, 1.0
	v_fma_f32 v13, v152, v13, 1.0
	v_fma_f32 v5, v152, v5, 1.0
	v_mul_f32_e32 v51, v87, v86
	v_mul_f32_e32 v60, v60, v88
	v_mul_f32_e32 v13, v13, v48
	v_mul_f32_e32 v5, v5, v8
	v_mul_f32_e32 v51, v12, v51
	v_mul_f32_e32 v12, v12, v60
	v_cvt_pk_bf16_f32 v60, v51, v12
	v_mul_f32_e32 v14, v50, v14
	v_mul_f32_e32 v13, v50, v13
	v_cvt_pk_bf16_f32 v48, v14, v13
	v_mul_f32_e32 v6, v6, v11
	v_mul_f32_e32 v8, v11, v5
	v_cvt_pk_bf16_f32 v5, v6, v8
	v_mul_f32_e32 v4, v9, v4
	ds_write_b16 v97, v60 offset:6784
	ds_write_b16_d16_hi v97, v60 offset:9088
	ds_write_b16 v97, v48 offset:6928
	ds_write_b16_d16_hi v97, v48 offset:9232
	ds_write_b16 v97, v5 offset:7072
	ds_write_b16_d16_hi v97, v5 offset:9376
	v_rcp_f32_e32 v5, v4
	v_mul_f32_e32 v2, v2, v0
	v_add_f32_e32 v0, -1.0, v0
	v_fma_f32 v0, v152, v0, 1.0
	v_mul_f32_e32 v0, v0, v3
	s_waitcnt lgkmcnt(14)
	v_lshlrev_b32_e32 v89, 16, v182
	v_mul_f32_e32 v9, v2, v5
	v_mul_f32_e32 v0, v5, v0
	v_cvt_pk_bf16_f32 v2, v9, v0
	ds_write_b16 v97, v2 offset:7216
	ds_write_b16_d16_hi v97, v2 offset:9520
	v_mul_f32_e32 v2, v4, v89
	v_rcp_f32_e32 v3, v2
	v_lshlrev_b32_e32 v91, 16, v198
	v_lshlrev_b32_e32 v92, 16, v190
	v_mul_f32_e32 v4, v92, v91
	v_mul_f32_e32 v11, v3, v4
	v_add_f32_e32 v4, -1.0, v91
	v_lshlrev_b32_e32 v95, 16, v206
	v_fma_f32 v4, v152, v4, 1.0
	v_and_b32_e32 v52, 0xffff0000, v182
	v_mul_f32_e32 v4, v4, v95
	v_mul_f32_e32 v48, v3, v4
	v_cvt_pk_bf16_f32 v3, v11, v48
	v_mul_f32_e32 v2, v2, v52
	ds_write_b16 v97, v3 offset:7360
	ds_write_b16_d16_hi v97, v3 offset:9664
	v_rcp_f32_e32 v3, v2
	v_and_b32_e32 v54, 0xffff0000, v198
	v_and_b32_e32 v56, 0xffff0000, v190
	v_mul_f32_e32 v4, v56, v54
	v_mul_f32_e32 v50, v3, v4
	v_add_f32_e32 v4, -1.0, v54
	v_and_b32_e32 v58, 0xffff0000, v206
	v_fma_f32 v4, v152, v4, 1.0
	v_lshlrev_b32_e32 v90, 16, v183
	v_mul_f32_e32 v4, v4, v58
	v_mul_f32_e32 v52, v3, v4
	v_cvt_pk_bf16_f32 v3, v50, v52
	v_mul_f32_e32 v2, v2, v90
	ds_write_b16 v97, v3 offset:7504
	ds_write_b16_d16_hi v97, v3 offset:9808
	v_rcp_f32_e32 v3, v2
	v_lshlrev_b32_e32 v93, 16, v199
	v_lshlrev_b32_e32 v94, 16, v191
	v_and_b32_e32 v53, 0xffff0000, v183
	v_mul_f32_e32 v4, v94, v93
	v_mul_f32_e32 v54, v4, v3
	v_add_f32_e32 v4, -1.0, v93
	v_mul_f32_e32 v2, v2, v53
	v_lshlrev_b32_e32 v96, 16, v207
	v_fma_f32 v4, v152, v4, 1.0
	v_rcp_f32_e32 v2, v2
	v_mul_f32_e32 v4, v4, v96
	v_and_b32_e32 v55, 0xffff0000, v199
	v_and_b32_e32 v57, 0xffff0000, v191
	v_mul_f32_e32 v56, v3, v4
	v_cvt_pk_bf16_f32 v3, v54, v56
	ds_write_b16 v97, v3 offset:7648
	ds_write_b16_d16_hi v97, v3 offset:9952
	v_mul_f32_e32 v3, v57, v55
	v_mul_f32_e32 v53, v3, v2
	v_add_f32_e32 v3, -1.0, v55
	v_and_b32_e32 v59, 0xffff0000, v207
	v_fma_f32 v3, v152, v3, 1.0
	v_mul_f32_e32 v3, v3, v59
	v_mul_f32_e32 v55, v2, v3
	v_cvt_pk_bf16_f32 v2, v53, v55
	ds_write_b16 v97, v2 offset:7792
	ds_write_b16_d16_hi v97, v2 offset:10096
	v_add_u32_e32 v57, s10, v133
	v_cvt_pk_bf16_f32 v2, v65, v67
	v_cvt_pk_bf16_f32 v3, v66, v68
	v_cvt_pk_bf16_f32 v4, v70, v72
	v_cvt_pk_bf16_f32 v5, v49, v10
	ds_write_b128 v57, v[2:5] offset:10240
	v_cvt_pk_bf16_f32 v2, v51, v14
	v_cvt_pk_bf16_f32 v3, v6, v9
	v_cvt_pk_bf16_f32 v4, v11, v50
	v_cvt_pk_bf16_f32 v5, v54, v53
	ds_write_b128 v57, v[2:5] offset:10256
	v_cvt_pk_bf16_f32 v2, v64, v61
	v_cvt_pk_bf16_f32 v3, v62, v63
	v_cvt_pk_bf16_f32 v4, v69, v71
	v_cvt_pk_bf16_f32 v5, v15, v7
	ds_write_b128 v57, v[2:5] offset:10272
	v_cvt_pk_bf16_f32 v2, v12, v13
	v_cvt_pk_bf16_f32 v3, v8, v0
	v_cvt_pk_bf16_f32 v4, v48, v52
	v_cvt_pk_bf16_f32 v5, v56, v55
	ds_write_b128 v57, v[2:5] offset:10288

.LBB0_964:
	s_andn2_b64 vcc, exec, s[10:11]
	s_cbranch_vccnz .LBB0_967
	s_cmpk_gt_u32 s84, 0xfe
	s_cbranch_scc1 .LBB0_967
	v_add_u32_e32 v2, s70, v126
	v_add_u32_e32 v0, 16, v2
	v_add_u32_e32 v2, 24, v2
	v_cndmask_b32_e64 v0, v115, v0, s[60:61]
	v_cndmask_b32_e64 v2, v117, v2, s[60:61]
	v_add_u32_e32 v0, s20, v0
	v_add_u32_e32 v2, s20, v2
	s_movk_i32 s12, 0x2800
	v_lshlrev_b64 v[4:5], 13, v[0:1]
	v_mad_u64_u32 v[56:57], s[10:11], v0, s12, v[120:121]
	v_mad_u64_u32 v[58:59], s[10:11], v2, s12, v[120:121]
	v_mov_b32_e32 v3, v1
	v_lshl_add_u64 v[14:15], v[118:119], 0, v[4:5]
	s_movk_i32 s10, 0x1000
	v_lshlrev_b64 v[4:5], 13, v[2:3]
	v_add_co_u32_e32 v10, vcc, s10, v14
	v_lshl_add_u64 v[64:65], v[118:119], 0, v[4:5]
	s_nop 0
	v_addc_co_u32_e32 v11, vcc, 0, v15, vcc
	v_add_co_u32_e32 v48, vcc, s10, v64
	global_load_dwordx4 v[2:5], v[56:57], off nt
	global_load_dwordx4 v[6:9], v[58:59], off nt
	v_addc_co_u32_e32 v49, vcc, 0, v65, vcc
	global_load_dwordx4 v[10:13], v[10:11], off offset:2048 nt
	s_nop 0
	global_load_dwordx4 v[48:51], v[48:49], off offset:2048 nt
	s_nop 0
	global_load_dwordx4 v[52:55], v[14:15], off offset:2048 nt
	v_add_co_u32_e32 v14, vcc, s10, v58
	s_nop 1
	v_addc_co_u32_e32 v15, vcc, 0, v59, vcc
	v_add_co_u32_e32 v60, vcc, 0x1000, v56
	s_nop 1
	v_addc_co_u32_e32 v61, vcc, 0, v57, vcc
	global_load_dwordx4 v[56:59], v[14:15], off nt
	s_nop 0
	global_load_dwordx4 v[60:63], v[60:61], off nt
	s_nop 0
	global_load_dwordx4 v[64:67], v[64:65], off offset:2048 nt
	s_waitcnt vmcnt(0)
	s_waitcnt vmcnt(7)
	ds_write_b128 v151, v[2:5]
	s_waitcnt vmcnt(6)
	ds_write_b128 v151, v[6:9] offset:1024
	s_waitcnt vmcnt(3)
	ds_write_b128 v151, v[52:55] offset:6144
	ds_write_b128 v151, v[10:13] offset:2048
	ds_write_b128 v151, v[48:51] offset:3072
	s_waitcnt vmcnt(2)
	ds_write_b128 v151, v[56:59] offset:5120
	s_waitcnt vmcnt(1)
	ds_write_b128 v151, v[60:63] offset:4096
	s_waitcnt vmcnt(0)
	ds_write_b128 v151, v[64:67] offset:7168
	v_add_u32_e32 v208, s29, v129
	ds_read_b64_tr_b16 v[176:177], v208
	ds_read_b64_tr_b16 v[178:179], v208 offset:512
	ds_read_b64_tr_b16 v[180:181], v208 offset:1024
	ds_read_b64_tr_b16 v[182:183], v208 offset:1536
	ds_read_b64_tr_b16 v[184:185], v208 offset:2048
	ds_read_b64_tr_b16 v[186:187], v208 offset:2560
	ds_read_b64_tr_b16 v[188:189], v208 offset:3072
	ds_read_b64_tr_b16 v[190:191], v208 offset:3584
	ds_read_b64_tr_b16 v[192:193], v208 offset:4096
	ds_read_b64_tr_b16 v[194:195], v208 offset:4608
	ds_read_b64_tr_b16 v[196:197], v208 offset:5120
	ds_read_b64_tr_b16 v[198:199], v208 offset:5632
	ds_read_b64_tr_b16 v[200:201], v208 offset:6144
	ds_read_b64_tr_b16 v[202:203], v208 offset:6656
	ds_read_b64_tr_b16 v[204:205], v208 offset:7168
	ds_read_b64_tr_b16 v[206:207], v208 offset:7680
	s_waitcnt lgkmcnt(0)
.LBB0_967:
	s_branch .LBB0_951
.LBB0_968:
	s_mov_b64 s[12:13], 0

.LBB0_978:
	s_andn2_b64 vcc, exec, s[8:9]
	s_cbranch_vccnz .LBB0_981
	s_cmpk_gt_u32 s84, 0xfe
	s_cbranch_scc1 .LBB0_981
	v_add_u32_e32 v2, s70, v126
	v_add_u32_e32 v0, 16, v2
	v_cndmask_b32_e64 v0, v115, v0, s[60:61]
	v_add_u32_e32 v2, 24, v2
	v_add_u32_e32 v0, s20, v0
	v_cndmask_b32_e64 v2, v117, v2, s[60:61]
	v_add_u32_e32 v2, s20, v2
	v_mov_b32_e32 v3, v1
	v_lshlrev_b64 v[4:5], 13, v[0:1]
	v_lshl_add_u64 v[14:15], v[118:119], 0, v[4:5]
	v_lshlrev_b64 v[4:5], 13, v[2:3]
	s_movk_i32 s12, 0x2800
	v_lshl_add_u64 v[56:57], v[118:119], 0, v[4:5]
	v_mad_u64_u32 v[4:5], s[8:9], v0, s12, v[120:121]
	v_mad_u64_u32 v[6:7], s[8:9], v2, s12, v[120:121]
	s_movk_i32 s8, 0x1000
	s_nop 0
	v_add_co_u32_e32 v60, vcc, s8, v14
	global_load_dwordx4 v[2:5], v[4:5], off nt
	s_nop 0
	global_load_dwordx4 v[6:9], v[6:7], off nt
	v_addc_co_u32_e32 v61, vcc, 0, v15, vcc
	global_load_dwordx4 v[10:13], v[60:61], off offset:2048 nt
	global_load_dwordx4 v[48:51], v[56:57], off nt
	global_load_dwordx4 v[52:55], v[14:15], off nt
	v_add_co_u32_e32 v14, vcc, s8, v56
	s_nop 1
	v_addc_co_u32_e32 v15, vcc, 0, v57, vcc
	global_load_dwordx4 v[56:59], v[14:15], off offset:2048 nt
	s_nop 0
	global_load_dwordx4 v[60:63], v[60:61], off nt
	s_nop 0
	global_load_dwordx4 v[64:67], v[14:15], off nt
	s_waitcnt vmcnt(0)
	s_waitcnt vmcnt(7)
	ds_write_b128 v151, v[2:5]
	s_waitcnt vmcnt(6)
	ds_write_b128 v151, v[6:9] offset:1024
	s_waitcnt vmcnt(3)
	ds_write_b128 v151, v[52:55] offset:4096
	ds_write_b128 v151, v[48:51] offset:5120
	ds_write_b128 v151, v[10:13] offset:2048
	s_waitcnt vmcnt(2)
	ds_write_b128 v151, v[56:59] offset:3072
	s_waitcnt vmcnt(1)
	ds_write_b128 v151, v[60:63] offset:6144
	s_waitcnt vmcnt(0)
	ds_write_b128 v151, v[64:67] offset:7168
	v_add_u32_e32 v208, s29, v129
	ds_read_b64_tr_b16 v[176:177], v208
	ds_read_b64_tr_b16 v[178:179], v208 offset:512
	ds_read_b64_tr_b16 v[180:181], v208 offset:1024
	ds_read_b64_tr_b16 v[182:183], v208 offset:1536
	ds_read_b64_tr_b16 v[184:185], v208 offset:2048
	ds_read_b64_tr_b16 v[186:187], v208 offset:2560
	ds_read_b64_tr_b16 v[188:189], v208 offset:3072
	ds_read_b64_tr_b16 v[190:191], v208 offset:3584
	ds_read_b64_tr_b16 v[192:193], v208 offset:4096
	ds_read_b64_tr_b16 v[194:195], v208 offset:4608
	ds_read_b64_tr_b16 v[196:197], v208 offset:5120
	ds_read_b64_tr_b16 v[198:199], v208 offset:5632
	ds_read_b64_tr_b16 v[200:201], v208 offset:6144
	ds_read_b64_tr_b16 v[202:203], v208 offset:6656
	ds_read_b64_tr_b16 v[204:205], v208 offset:7168
	ds_read_b64_tr_b16 v[206:207], v208 offset:7680
	s_waitcnt lgkmcnt(0)
.LBB0_981:
	s_branch .LBB0_951
.LBB0_982:
	s_andn2_b64 vcc, exec, s[12:13]
	s_cbranch_vccnz .LBB0_993
	s_add_i32 s8, s84, -1
	s_cmpk_gt_u32 s8, 0xff
	s_cbranch_scc1 .LBB0_993
	s_mul_i32 s9, s8, 0xab
	s_bfe_u32 s9, s9, 0x70009
	s_mul_i32 s9, s9, 3
	s_sub_i32 s8, s8, s9
	s_and_b32 s8, s8, 0xff
	s_mulk_i32 s8, 0x5300
	s_add_i32 s12, s8, 0
	v_add3_u32 v10, s12, v135, v136
	ds_read_b128 v[2:5], v10 offset:5632
	v_add_u32_e32 v0, s12, v137
	v_add_u32_e32 v11, v0, v136
	ds_read_b128 v[6:9], v11
	s_waitcnt lgkmcnt(0)
	v_mfma_f32_32x32x16_bf16 v[48:63], v[2:5], v[6:9], 0
	ds_read_b128 v[2:5], v10 offset:5664
	ds_read_b128 v[6:9], v11 offset:32
	s_waitcnt lgkmcnt(0)
	v_mfma_f32_32x32x16_bf16 v[48:63], v[2:5], v[6:9], v[48:63]
	ds_read_b128 v[2:5], v10 offset:5696
	ds_read_b128 v[6:9], v11 offset:64
	s_waitcnt lgkmcnt(0)
	v_mfma_f32_32x32x16_bf16 v[48:63], v[2:5], v[6:9], v[48:63]
	ds_read_b128 v[2:5], v10 offset:5728
	ds_read_b128 v[6:9], v11 offset:96
	s_waitcnt lgkmcnt(0)
	v_mfma_f32_32x32x16_bf16 v[48:63], v[2:5], v[6:9], v[48:63]
	s_nop 11
	v_cndmask_b32_e64 v3, 0, v48, s[44:45]
	v_cndmask_b32_e64 v4, 0, v49, s[46:47]
	s_and_saveexec_b64 s[8:9], s[40:41]
	s_xor_b64 s[8:9], exec, s[8:9]
	s_cbranch_execz .LBB0_986
	v_cvt_pk_bf16_f32 v2, v3, v4

.LBB0_1005:
	s_cmp_gt_i32 s84, 1
	s_cselect_b64 s[4:5], -1, 0
.LBB0_1006:
	s_andn2_b64 vcc, exec, s[4:5]
	s_cbranch_vccnz .LBB0_951
	s_branch .Lscan_seq_go
.Lscan_fast_seq:
	s_cmp_gt_i32 s84, 1
	s_cbranch_scc0 .LBB0_951
	s_cmpk_lt_i32 s84, 0x102
	s_cbranch_scc0 .LBB0_951
.Lscan_seq_go:
	s_add_i32 s4, s84, 0xfffe
	s_and_b32 s5, s4, 0xffff
	s_mul_i32 s5, s5, 0xaaab
	s_lshr_b32 s5, s5, 17
	s_mul_i32 s5, s5, 3
	s_sub_i32 s4, s4, s5
	s_and_b32 s4, s4, 0xffff
	s_mulk_i32 s4, 0x5300
	s_add_i32 s4, s4, 0
	v_add3_u32 v0, s4, v137, v136
	ds_read_b128 v[2:5], v0
	v_cvt_pk_bf16_f32 v6, v16, v17
	v_cvt_pk_bf16_f32 v7, v18, v19
	v_cvt_pk_bf16_f32 v8, v20, v21
	v_cvt_pk_bf16_f32 v9, v22, v23
	ds_read_b128 v[10:13], v0 offset:32
	ds_read_b128 v[68:71], v0 offset:64
	ds_read_b128 v[76:79], v0 offset:96
	v_add3_u32 v14, s4, v142, v136
	ds_read_b128 v[104:107], v0 offset:128
	ds_read_b128 v[64:67], v14 offset:15360
	v_add3_u32 v0, s4, v140, v136
	s_waitcnt lgkmcnt(5)
	v_mfma_f32_32x32x16_bf16 v[48:63], v[2:5], v[6:9], 0
	v_cvt_pk_bf16_f32 v2, v24, v25
	v_cvt_pk_bf16_f32 v3, v26, v27
	v_cvt_pk_bf16_f32 v4, v28, v29
	v_cvt_pk_bf16_f32 v5, v30, v31
	v_lshl_add_u32 v111, v128, 2, s4
	v_add3_u32 v6, s4, v143, v136
	ds_read_b128 v[100:103], v0 offset:18432
	ds_read_b128 v[92:95], v6 offset:10240
	ds_read_b128 v[88:91], v6 offset:10272
	ds_read_b128 v[80:83], v6 offset:12800
	s_waitcnt lgkmcnt(8)
	v_mfma_f32_32x32x16_bf16 v[48:63], v[10:13], v[2:5], v[48:63]
	v_cvt_pk_bf16_f32 v2, v32, v33
	v_cvt_pk_bf16_f32 v3, v34, v35
	v_cvt_pk_bf16_f32 v4, v36, v37
	v_cvt_pk_bf16_f32 v5, v38, v39
	v_lshl_add_u32 v110, v138, 2, s4
	v_add_u32_e32 v108, 0x4c00, v111
	s_waitcnt lgkmcnt(7)
	v_mfma_f32_32x32x16_bf16 v[48:63], v[68:71], v[2:5], v[48:63]
	v_cvt_pk_bf16_f32 v2, v40, v41
	v_cvt_pk_bf16_f32 v3, v42, v43
	v_cvt_pk_bf16_f32 v4, v44, v45
	v_cvt_pk_bf16_f32 v5, v46, v47
	ds_read_b128 v[68:71], v6 offset:12832
	ds_read_b128 v[72:75], v110 offset:20992
	s_waitcnt lgkmcnt(8)
	v_mfma_f32_32x32x16_bf16 v[48:63], v[76:79], v[2:5], v[48:63]
	ds_read_b128 v[76:79], v110 offset:21024
	ds_read_b128 v[84:87], v110 offset:21056
	ds_read_b128 v[6:9], v110 offset:21152
	ds_read_b128 v[10:13], v110 offset:21184
	ds_read_b128 v[2:5], v110 offset:21120
	ds_read_b128 v[96:99], v110 offset:21088
	s_waitcnt lgkmcnt(12)
	v_mfma_f32_32x32x16_bf16 v[48:63], v[104:107], v[64:67], v[48:63]
	ds_read2_b32 v[168:169], v108 offset0:128 offset1:144
	ds_read2_b32 v[170:171], v108 offset0:160 offset1:176
	ds_read2_b32 v[172:173], v108 offset0:192 offset1:208
	ds_read2_b32 v[174:175], v108 offset0:224 offset1:240
	v_add_u32_e32 v176, 0x5000, v111
	ds_read2_b32 v[178:179], v176 offset1:16
	ds_read2_b32 v[180:181], v176 offset0:32 offset1:48
	ds_read2_b32 v[182:183], v176 offset0:64 offset1:80
	ds_read_b32 v184, v111 offset:20864
	ds_read_b128 v[104:107], v110 offset:21216
	s_nop 1
	v_mov_b32_e32 v0, v48
	v_mov_b32_e32 v15, v49
	v_mov_b32_e32 v155, v50
	v_mov_b32_e32 v157, v51
	v_mov_b32_e32 v159, v52
	v_mov_b32_e32 v160, v53
	v_mov_b32_e32 v161, v54
	v_mov_b32_e32 v165, v55
	v_permlane32_swap_b32_e32 v48, v0
	v_permlane32_swap_b32_e32 v49, v15
	v_permlane32_swap_b32_e32 v50, v155
	v_permlane32_swap_b32_e32 v51, v157
	v_permlane32_swap_b32_e32 v52, v159
	v_permlane32_swap_b32_e32 v53, v160
	v_permlane32_swap_b32_e32 v54, v161
	v_permlane32_swap_b32_e32 v55, v165
	s_waitcnt lgkmcnt(0)
	v_fmac_f32_dpp v49, v168, v48 row_newbcast:1 row_mask:0xf bank_mask:0xf
	v_fmac_f32_dpp v50, v168, v48 row_newbcast:2 row_mask:0xf bank_mask:0xf
	v_fmac_f32_dpp v51, v168, v48 row_newbcast:3 row_mask:0xf bank_mask:0xf
	v_fmac_f32_dpp v0, v168, v48 row_newbcast:4 row_mask:0xf bank_mask:0xf
	v_fmac_f32_dpp v15, v168, v48 row_newbcast:5 row_mask:0xf bank_mask:0xf
	v_fmac_f32_dpp v155, v168, v48 row_newbcast:6 row_mask:0xf bank_mask:0xf
	v_fmac_f32_dpp v157, v168, v48 row_newbcast:7 row_mask:0xf bank_mask:0xf
	v_fmac_f32_dpp v52, v168, v48 row_newbcast:8 row_mask:0xf bank_mask:0xf
	v_fmac_f32_dpp v53, v168, v48 row_newbcast:9 row_mask:0xf bank_mask:0xf
	v_fmac_f32_dpp v54, v168, v48 row_newbcast:10 row_mask:0xf bank_mask:0xf
	v_fmac_f32_dpp v55, v168, v48 row_newbcast:11 row_mask:0xf bank_mask:0xf
	v_fmac_f32_dpp v159, v168, v48 row_newbcast:12 row_mask:0xf bank_mask:0xf
	v_fmac_f32_dpp v160, v168, v48 row_newbcast:13 row_mask:0xf bank_mask:0xf
	v_fmac_f32_dpp v161, v168, v48 row_newbcast:14 row_mask:0xf bank_mask:0xf
	v_fmac_f32_dpp v165, v168, v48 row_newbcast:15 row_mask:0xf bank_mask:0xf
	v_fmac_f32_dpp v50, v169, v49 row_newbcast:2 row_mask:0xf bank_mask:0xf
	v_fmac_f32_dpp v51, v169, v49 row_newbcast:3 row_mask:0xf bank_mask:0xf
	v_fmac_f32_dpp v0, v169, v49 row_newbcast:4 row_mask:0xf bank_mask:0xf
	v_fmac_f32_dpp v15, v169, v49 row_newbcast:5 row_mask:0xf bank_mask:0xf
	v_fmac_f32_dpp v155, v169, v49 row_newbcast:6 row_mask:0xf bank_mask:0xf
	v_fmac_f32_dpp v157, v169, v49 row_newbcast:7 row_mask:0xf bank_mask:0xf
	v_fmac_f32_dpp v52, v169, v49 row_newbcast:8 row_mask:0xf bank_mask:0xf
	v_fmac_f32_dpp v53, v169, v49 row_newbcast:9 row_mask:0xf bank_mask:0xf
	v_fmac_f32_dpp v54, v169, v49 row_newbcast:10 row_mask:0xf bank_mask:0xf
	v_fmac_f32_dpp v55, v169, v49 row_newbcast:11 row_mask:0xf bank_mask:0xf
	v_fmac_f32_dpp v159, v169, v49 row_newbcast:12 row_mask:0xf bank_mask:0xf
	v_fmac_f32_dpp v160, v169, v49 row_newbcast:13 row_mask:0xf bank_mask:0xf
	v_fmac_f32_dpp v161, v169, v49 row_newbcast:14 row_mask:0xf bank_mask:0xf
	v_fmac_f32_dpp v165, v169, v49 row_newbcast:15 row_mask:0xf bank_mask:0xf
	v_fmac_f32_dpp v51, v170, v50 row_newbcast:3 row_mask:0xf bank_mask:0xf
	v_fmac_f32_dpp v0, v170, v50 row_newbcast:4 row_mask:0xf bank_mask:0xf
	v_fmac_f32_dpp v15, v170, v50 row_newbcast:5 row_mask:0xf bank_mask:0xf
	v_fmac_f32_dpp v155, v170, v50 row_newbcast:6 row_mask:0xf bank_mask:0xf
	v_fmac_f32_dpp v157, v170, v50 row_newbcast:7 row_mask:0xf bank_mask:0xf
	v_fmac_f32_dpp v52, v170, v50 row_newbcast:8 row_mask:0xf bank_mask:0xf
	v_fmac_f32_dpp v53, v170, v50 row_newbcast:9 row_mask:0xf bank_mask:0xf
	v_fmac_f32_dpp v54, v170, v50 row_newbcast:10 row_mask:0xf bank_mask:0xf
	v_fmac_f32_dpp v55, v170, v50 row_newbcast:11 row_mask:0xf bank_mask:0xf
	v_fmac_f32_dpp v159, v170, v50 row_newbcast:12 row_mask:0xf bank_mask:0xf
	v_fmac_f32_dpp v160, v170, v50 row_newbcast:13 row_mask:0xf bank_mask:0xf
	v_fmac_f32_dpp v161, v170, v50 row_newbcast:14 row_mask:0xf bank_mask:0xf
	v_fmac_f32_dpp v165, v170, v50 row_newbcast:15 row_mask:0xf bank_mask:0xf
	v_fmac_f32_dpp v0, v171, v51 row_newbcast:4 row_mask:0xf bank_mask:0xf
	v_fmac_f32_dpp v15, v171, v51 row_newbcast:5 row_mask:0xf bank_mask:0xf
	v_fmac_f32_dpp v155, v171, v51 row_newbcast:6 row_mask:0xf bank_mask:0xf
	v_fmac_f32_dpp v157, v171, v51 row_newbcast:7 row_mask:0xf bank_mask:0xf
	v_fmac_f32_dpp v52, v171, v51 row_newbcast:8 row_mask:0xf bank_mask:0xf
	v_fmac_f32_dpp v53, v171, v51 row_newbcast:9 row_mask:0xf bank_mask:0xf
	v_fmac_f32_dpp v54, v171, v51 row_newbcast:10 row_mask:0xf bank_mask:0xf
	v_fmac_f32_dpp v55, v171, v51 row_newbcast:11 row_mask:0xf bank_mask:0xf
	v_fmac_f32_dpp v159, v171, v51 row_newbcast:12 row_mask:0xf bank_mask:0xf
	v_fmac_f32_dpp v160, v171, v51 row_newbcast:13 row_mask:0xf bank_mask:0xf
	v_fmac_f32_dpp v161, v171, v51 row_newbcast:14 row_mask:0xf bank_mask:0xf
	v_fmac_f32_dpp v165, v171, v51 row_newbcast:15 row_mask:0xf bank_mask:0xf
	v_fmac_f32_dpp v15, v172, v0 row_newbcast:5 row_mask:0xf bank_mask:0xf
	v_fmac_f32_dpp v155, v172, v0 row_newbcast:6 row_mask:0xf bank_mask:0xf
	v_fmac_f32_dpp v157, v172, v0 row_newbcast:7 row_mask:0xf bank_mask:0xf
	v_fmac_f32_dpp v52, v172, v0 row_newbcast:8 row_mask:0xf bank_mask:0xf
	v_fmac_f32_dpp v53, v172, v0 row_newbcast:9 row_mask:0xf bank_mask:0xf
	v_fmac_f32_dpp v54, v172, v0 row_newbcast:10 row_mask:0xf bank_mask:0xf
	v_fmac_f32_dpp v55, v172, v0 row_newbcast:11 row_mask:0xf bank_mask:0xf
	v_fmac_f32_dpp v159, v172, v0 row_newbcast:12 row_mask:0xf bank_mask:0xf
	v_fmac_f32_dpp v160, v172, v0 row_newbcast:13 row_mask:0xf bank_mask:0xf
	v_fmac_f32_dpp v161, v172, v0 row_newbcast:14 row_mask:0xf bank_mask:0xf
	v_fmac_f32_dpp v165, v172, v0 row_newbcast:15 row_mask:0xf bank_mask:0xf
	v_fmac_f32_dpp v155, v173, v15 row_newbcast:6 row_mask:0xf bank_mask:0xf
	v_fmac_f32_dpp v157, v173, v15 row_newbcast:7 row_mask:0xf bank_mask:0xf
	v_fmac_f32_dpp v52, v173, v15 row_newbcast:8 row_mask:0xf bank_mask:0xf
	v_fmac_f32_dpp v53, v173, v15 row_newbcast:9 row_mask:0xf bank_mask:0xf
	v_fmac_f32_dpp v54, v173, v15 row_newbcast:10 row_mask:0xf bank_mask:0xf
	v_fmac_f32_dpp v55, v173, v15 row_newbcast:11 row_mask:0xf bank_mask:0xf
	v_fmac_f32_dpp v159, v173, v15 row_newbcast:12 row_mask:0xf bank_mask:0xf
	v_fmac_f32_dpp v160, v173, v15 row_newbcast:13 row_mask:0xf bank_mask:0xf
	v_fmac_f32_dpp v161, v173, v15 row_newbcast:14 row_mask:0xf bank_mask:0xf
	v_fmac_f32_dpp v165, v173, v15 row_newbcast:15 row_mask:0xf bank_mask:0xf
	v_fmac_f32_dpp v157, v174, v155 row_newbcast:7 row_mask:0xf bank_mask:0xf
	v_fmac_f32_dpp v52, v174, v155 row_newbcast:8 row_mask:0xf bank_mask:0xf
	v_fmac_f32_dpp v53, v174, v155 row_newbcast:9 row_mask:0xf bank_mask:0xf
	v_fmac_f32_dpp v54, v174, v155 row_newbcast:10 row_mask:0xf bank_mask:0xf
	v_fmac_f32_dpp v55, v174, v155 row_newbcast:11 row_mask:0xf bank_mask:0xf
	v_fmac_f32_dpp v159, v174, v155 row_newbcast:12 row_mask:0xf bank_mask:0xf
	v_fmac_f32_dpp v160, v174, v155 row_newbcast:13 row_mask:0xf bank_mask:0xf
	v_fmac_f32_dpp v161, v174, v155 row_newbcast:14 row_mask:0xf bank_mask:0xf
	v_fmac_f32_dpp v165, v174, v155 row_newbcast:15 row_mask:0xf bank_mask:0xf
	v_fmac_f32_dpp v52, v175, v157 row_newbcast:8 row_mask:0xf bank_mask:0xf
	v_fmac_f32_dpp v53, v175, v157 row_newbcast:9 row_mask:0xf bank_mask:0xf
	v_fmac_f32_dpp v54, v175, v157 row_newbcast:10 row_mask:0xf bank_mask:0xf
	v_fmac_f32_dpp v55, v175, v157 row_newbcast:11 row_mask:0xf bank_mask:0xf
	v_fmac_f32_dpp v159, v175, v157 row_newbcast:12 row_mask:0xf bank_mask:0xf
	v_fmac_f32_dpp v160, v175, v157 row_newbcast:13 row_mask:0xf bank_mask:0xf
	v_fmac_f32_dpp v161, v175, v157 row_newbcast:14 row_mask:0xf bank_mask:0xf
	v_fmac_f32_dpp v165, v175, v157 row_newbcast:15 row_mask:0xf bank_mask:0xf
	v_fmac_f32_dpp v53, v178, v52 row_newbcast:9 row_mask:0xf bank_mask:0xf
	v_fmac_f32_dpp v54, v178, v52 row_newbcast:10 row_mask:0xf bank_mask:0xf
	v_fmac_f32_dpp v55, v178, v52 row_newbcast:11 row_mask:0xf bank_mask:0xf
	v_fmac_f32_dpp v159, v178, v52 row_newbcast:12 row_mask:0xf bank_mask:0xf
	v_fmac_f32_dpp v160, v178, v52 row_newbcast:13 row_mask:0xf bank_mask:0xf
	v_fmac_f32_dpp v161, v178, v52 row_newbcast:14 row_mask:0xf bank_mask:0xf
	v_fmac_f32_dpp v165, v178, v52 row_newbcast:15 row_mask:0xf bank_mask:0xf
	v_fmac_f32_dpp v54, v179, v53 row_newbcast:10 row_mask:0xf bank_mask:0xf
	v_fmac_f32_dpp v55, v179, v53 row_newbcast:11 row_mask:0xf bank_mask:0xf
	v_fmac_f32_dpp v159, v179, v53 row_newbcast:12 row_mask:0xf bank_mask:0xf
	v_fmac_f32_dpp v160, v179, v53 row_newbcast:13 row_mask:0xf bank_mask:0xf
	v_fmac_f32_dpp v161, v179, v53 row_newbcast:14 row_mask:0xf bank_mask:0xf
	v_fmac_f32_dpp v165, v179, v53 row_newbcast:15 row_mask:0xf bank_mask:0xf
	v_fmac_f32_dpp v55, v180, v54 row_newbcast:11 row_mask:0xf bank_mask:0xf
	v_fmac_f32_dpp v159, v180, v54 row_newbcast:12 row_mask:0xf bank_mask:0xf
	v_fmac_f32_dpp v160, v180, v54 row_newbcast:13 row_mask:0xf bank_mask:0xf
	v_fmac_f32_dpp v161, v180, v54 row_newbcast:14 row_mask:0xf bank_mask:0xf
	v_fmac_f32_dpp v165, v180, v54 row_newbcast:15 row_mask:0xf bank_mask:0xf
	v_fmac_f32_dpp v159, v181, v55 row_newbcast:12 row_mask:0xf bank_mask:0xf
	v_fmac_f32_dpp v160, v181, v55 row_newbcast:13 row_mask:0xf bank_mask:0xf
	v_fmac_f32_dpp v161, v181, v55 row_newbcast:14 row_mask:0xf bank_mask:0xf
	v_fmac_f32_dpp v165, v181, v55 row_newbcast:15 row_mask:0xf bank_mask:0xf
	v_fmac_f32_dpp v160, v182, v159 row_newbcast:13 row_mask:0xf bank_mask:0xf
	v_fmac_f32_dpp v161, v182, v159 row_newbcast:14 row_mask:0xf bank_mask:0xf
	v_fmac_f32_dpp v165, v182, v159 row_newbcast:15 row_mask:0xf bank_mask:0xf
	v_fmac_f32_dpp v161, v183, v160 row_newbcast:14 row_mask:0xf bank_mask:0xf
	v_fmac_f32_dpp v165, v183, v160 row_newbcast:15 row_mask:0xf bank_mask:0xf
	v_fmac_f32_dpp v165, v184, v161 row_newbcast:15 row_mask:0xf bank_mask:0xf
	s_mov_b64 s[4:5], exec
	s_andn2_b64 exec, s[4:5], s[42:43]
	v_cvt_pk_bf16_f32 v108, v48, v49
	v_cvt_pk_bf16_f32 v109, v50, v51
	v_cvt_pk_bf16_f32 v110, v0, v15
	v_cvt_pk_bf16_f32 v111, v155, v157
	s_and_b64 exec, s[4:5], s[42:43]
	v_cvt_pk_bf16_f32 v108, v52, v53
	v_cvt_pk_bf16_f32 v109, v54, v55
	v_cvt_pk_bf16_f32 v110, v159, v160
	v_cvt_pk_bf16_f32 v111, v161, v165
	s_mov_b64 exec, s[4:5]
	s_nop 1
	v_mfma_f32_32x32x16_bf16 v[48:63], v[100:103], v[108:111], v[48:63]
	v_mfma_f32_32x32x16_bf16 v[16:31], v[92:95], v[108:111], v[16:31]
	v_mfma_f32_32x32x16_bf16 v[32:47], v[80:83], v[108:111], v[32:47]
	v_mfma_f32_32x32x16_bf16 v[16:31], v[88:91], v[64:67], v[16:31]
	v_mfma_f32_32x32x16_bf16 v[32:47], v[68:71], v[64:67], v[32:47]
	s_add_i32 s4, s71, 0x3000
	s_and_b32 s4, s4, 0x1000
	v_add_u32_e32 v0, s4, v145
	v_add_u32_e32 v14, 0xf900, v0
	s_nop 3
	ds_write2st64_b32 v0, v56, v57 offset0:249 offset1:250
	ds_write2st64_b32 v0, v58, v59 offset0:251 offset1:252
	ds_write2st64_b32 v14, v60, v61 offset0:8 offset1:9
	ds_write2st64_b32 v14, v62, v63 offset0:10 offset1:11
	v_mul_f32_e64 v30, v98, v30
	v_mul_f32_e64 v31, v99, v31
	v_mul_f32_e64 v28, v96, v28
	v_mul_f32_e64 v29, v97, v29
	v_mul_f32_e64 v26, v86, v26
	v_mul_f32_e64 v27, v87, v27
	v_pk_mul_f32 v[24:25], v[84:85], v[24:25]
	v_pk_mul_f32 v[22:23], v[78:79], v[22:23]
	v_pk_mul_f32 v[20:21], v[76:77], v[20:21]
	v_pk_mul_f32 v[18:19], v[74:75], v[18:19]
	v_mul_f32_e64 v16, v72, v16
	v_mul_f32_e64 v17, v73, v17
	v_mul_f32_e64 v46, v106, v46
	v_mul_f32_e64 v47, v107, v47
	v_mul_f32_e64 v44, v104, v44
	v_mul_f32_e64 v45, v105, v45
	v_pk_mul_f32 v[42:43], v[12:13], v[42:43]
	v_pk_mul_f32 v[40:41], v[10:11], v[40:41]
	v_pk_mul_f32 v[38:39], v[8:9], v[38:39]
	v_pk_mul_f32 v[36:37], v[6:7], v[36:37]
	v_pk_mul_f32 v[34:35], v[4:5], v[34:35]
	v_pk_mul_f32 v[32:33], v[2:3], v[32:33]
	s_branch .LBB0_951
